# baseline layout, only change: sc0 sc1 nt on P0's 8 expert-weight stores (isolating write-through from the blocked layout)
# baseline (speedup 1.0000x reference)
; #define MOE_LOAD(v, it) do { _Pragma("unroll") for (int i_ = 0; i_ < 64; ++i_) v[i_] = __builtin_nontemporal_load((it).src + (size_t)(2 * i_) * (it).stride); } while (0)
;     ...
;         for (int j = 0; j < nmine; j += 2) {
;             const int it1 = gw + (j + 1) * NGW, it2 = gw + (j + 2) * NGW;
;             ib = moe_item(wg, wu, wd, win, wout, wpn, wpd, F.ws, it1 <= last ? it1 : last, F.lane); MOE_LOAD(vb, ib);
;             MOE_PROC(va, ia);
;             ia = moe_item(wg, wu, wd, win, wout, wpn, wpd, F.ws, it2 <= last ? it2 : last, F.lane); MOE_LOAD(va, ia);
;             MOE_PROC(vb, ib);
.LBB0_105:
	s_lshl_b64 s[46:47], s[46:47], 3
	global_load_dword v93, v[16:17], off nt
	v_lshl_add_u64 v[16:17], v[16:17], 0, s[46:47]
	v_lshl_add_u64 v[94:95], v[16:17], 0, s[46:47]
	v_lshl_add_u64 v[96:97], v[94:95], 0, s[46:47]
	v_lshl_add_u64 v[102:103], v[96:97], 0, s[46:47]
	v_lshl_add_u64 v[104:105], v[102:103], 0, s[46:47]
	v_lshl_add_u64 v[106:107], v[104:105], 0, s[46:47]
	v_lshl_add_u64 v[108:109], v[106:107], 0, s[46:47]
	v_lshl_add_u64 v[110:111], v[108:109], 0, s[46:47]
	global_load_dword v101, v[16:17], off nt
	global_load_dword v99, v[94:95], off nt
	global_load_dword v100, v[96:97], off nt
	s_nop 0
	global_load_dword v97, v[102:103], off nt
	global_load_dword v98, v[104:105], off nt
	global_load_dword v95, v[106:107], off nt
	global_load_dword v96, v[108:109], off nt
	global_load_dword v94, v[110:111], off nt
	v_lshl_add_u64 v[16:17], v[110:111], 0, s[46:47]
	s_waitcnt vmcnt(9)
	ds_write2st64_b32 v28, v87, v92 offset1:1
	v_lshl_add_u64 v[102:103], v[16:17], 0, s[46:47]
	global_load_dword v124, v[16:17], off nt
	global_load_dword v104, v[102:103], off nt
	v_lshl_add_u64 v[16:17], v[102:103], 0, s[46:47]
	global_load_dword v114, v[16:17], off nt
	v_lshl_add_u64 v[16:17], v[16:17], 0, s[46:47]
	global_load_dword v105, v[16:17], off nt
	v_lshl_add_u64 v[16:17], v[16:17], 0, s[46:47]
	global_load_dword v115, v[16:17], off nt
	v_lshl_add_u64 v[16:17], v[16:17], 0, s[46:47]
	global_load_dword v106, v[16:17], off nt
	v_lshl_add_u64 v[16:17], v[16:17], 0, s[46:47]
	global_load_dword v116, v[16:17], off nt
	v_lshl_add_u64 v[16:17], v[16:17], 0, s[46:47]
	global_load_dword v107, v[16:17], off nt
	v_lshl_add_u64 v[16:17], v[16:17], 0, s[46:47]
	global_load_dword v117, v[16:17], off nt
	v_lshl_add_u64 v[16:17], v[16:17], 0, s[46:47]
	global_load_dword v108, v[16:17], off nt
	v_lshl_add_u64 v[16:17], v[16:17], 0, s[46:47]
	global_load_dword v118, v[16:17], off nt
	v_lshl_add_u64 v[16:17], v[16:17], 0, s[46:47]
	global_load_dword v109, v[16:17], off nt
	v_lshl_add_u64 v[16:17], v[16:17], 0, s[46:47]
	global_load_dword v119, v[16:17], off nt
	v_lshl_add_u64 v[16:17], v[16:17], 0, s[46:47]
	global_load_dword v110, v[16:17], off nt
	v_lshl_add_u64 v[16:17], v[16:17], 0, s[46:47]
	global_load_dword v120, v[16:17], off nt
	v_lshl_add_u64 v[16:17], v[16:17], 0, s[46:47]
	global_load_dword v111, v[16:17], off nt
	v_lshl_add_u64 v[16:17], v[16:17], 0, s[46:47]
	global_load_dword v121, v[16:17], off nt
	v_lshl_add_u64 v[16:17], v[16:17], 0, s[46:47]
	global_load_dword v112, v[16:17], off nt
	v_lshl_add_u64 v[16:17], v[16:17], 0, s[46:47]
	global_load_dword v122, v[16:17], off nt
	v_lshl_add_u64 v[16:17], v[16:17], 0, s[46:47]
	global_load_dword v102, v[16:17], off nt
	v_lshl_add_u64 v[16:17], v[16:17], 0, s[46:47]
	global_load_dword v103, v[16:17], off nt
	v_lshl_add_u64 v[16:17], v[16:17], 0, s[46:47]
	global_load_dword v113, v[16:17], off nt
	v_lshl_add_u64 v[16:17], v[16:17], 0, s[46:47]
	global_load_dword v123, v[16:17], off nt
	v_lshl_add_u64 v[16:17], v[16:17], 0, s[46:47]
	global_load_dword v125, v[16:17], off nt
	v_lshl_add_u64 v[16:17], v[16:17], 0, s[46:47]
	global_load_dword v126, v[16:17], off nt
	v_lshl_add_u64 v[16:17], v[16:17], 0, s[46:47]
	global_load_dword v127, v[16:17], off nt
	v_lshl_add_u64 v[16:17], v[16:17], 0, s[46:47]
	global_load_dword v128, v[16:17], off nt
	v_lshl_add_u64 v[16:17], v[16:17], 0, s[46:47]
	global_load_dword v129, v[16:17], off nt
	v_lshl_add_u64 v[16:17], v[16:17], 0, s[46:47]
	global_load_dword v130, v[16:17], off nt
	v_lshl_add_u64 v[16:17], v[16:17], 0, s[46:47]
	global_load_dword v131, v[16:17], off nt
	v_lshl_add_u64 v[16:17], v[16:17], 0, s[46:47]
	global_load_dword v132, v[16:17], off nt
	v_lshl_add_u64 v[16:17], v[16:17], 0, s[46:47]
	global_load_dword v133, v[16:17], off nt
	v_lshl_add_u64 v[16:17], v[16:17], 0, s[46:47]
	global_load_dword v134, v[16:17], off nt
	v_lshl_add_u64 v[16:17], v[16:17], 0, s[46:47]
	global_load_dword v135, v[16:17], off nt
	v_lshl_add_u64 v[16:17], v[16:17], 0, s[46:47]
	global_load_dword v136, v[16:17], off nt
	v_lshl_add_u64 v[16:17], v[16:17], 0, s[46:47]
	global_load_dword v137, v[16:17], off nt
	v_lshl_add_u64 v[16:17], v[16:17], 0, s[46:47]
	global_load_dword v138, v[16:17], off nt
	v_lshl_add_u64 v[16:17], v[16:17], 0, s[46:47]
	global_load_dword v139, v[16:17], off nt
	v_lshl_add_u64 v[16:17], v[16:17], 0, s[46:47]
	global_load_dword v140, v[16:17], off nt
	v_lshl_add_u64 v[16:17], v[16:17], 0, s[46:47]
	global_load_dword v141, v[16:17], off nt
	v_lshl_add_u64 v[16:17], v[16:17], 0, s[46:47]
	global_load_dword v142, v[16:17], off nt
	v_lshl_add_u64 v[16:17], v[16:17], 0, s[46:47]
	global_load_dword v143, v[16:17], off nt
	v_lshl_add_u64 v[16:17], v[16:17], 0, s[46:47]
	global_load_dword v144, v[16:17], off nt
	v_lshl_add_u64 v[16:17], v[16:17], 0, s[46:47]
	global_load_dword v146, v[16:17], off nt
	v_lshl_add_u64 v[16:17], v[16:17], 0, s[46:47]
	global_load_dword v147, v[16:17], off nt
	v_lshl_add_u64 v[16:17], v[16:17], 0, s[46:47]
	global_load_dword v148, v[16:17], off nt
	v_lshl_add_u64 v[16:17], v[16:17], 0, s[46:47]
	global_load_dword v149, v[16:17], off nt
	v_lshl_add_u64 v[16:17], v[16:17], 0, s[46:47]
	global_load_dword v151, v[16:17], off nt
	v_lshl_add_u64 v[16:17], v[16:17], 0, s[46:47]
	global_load_dword v152, v[16:17], off nt
	v_lshl_add_u64 v[16:17], v[16:17], 0, s[46:47]
	global_load_dword v153, v[16:17], off nt
	v_lshl_add_u64 v[16:17], v[16:17], 0, s[46:47]
	global_load_dword v154, v[16:17], off nt
	v_lshl_add_u64 v[16:17], v[16:17], 0, s[46:47]
	global_load_dword v155, v[16:17], off nt
	v_lshl_add_u64 v[16:17], v[16:17], 0, s[46:47]
	global_load_dword v157, v[16:17], off nt
	v_lshl_add_u64 v[16:17], v[16:17], 0, s[46:47]
	global_load_dword v158, v[16:17], off nt
	v_lshl_add_u64 v[16:17], v[16:17], 0, s[46:47]
	ds_write2st64_b32 v28, v91, v90 offset0:2 offset1:3
	ds_write2st64_b32 v28, v89, v88 offset0:4 offset1:5
	ds_write2st64_b32 v28, v86, v85 offset0:6 offset1:7
	ds_write2st64_b32 v21, v83, v84 offset0:8 offset1:9
	ds_write2st64_b32 v21, v79, v80 offset0:10 offset1:11
	ds_write2st64_b32 v21, v75, v76 offset0:12 offset1:13
	ds_write2st64_b32 v21, v71, v72 offset0:14 offset1:15
	ds_write2st64_b32 v22, v65, v66 offset0:16 offset1:17
	ds_write2st64_b32 v22, v61, v62 offset0:18 offset1:19
	ds_write2st64_b32 v22, v57, v58 offset0:20 offset1:21
	ds_write2st64_b32 v22, v53, v54 offset0:22 offset1:23
	ds_write2st64_b32 v23, v45, v46 offset0:24 offset1:25
	ds_write2st64_b32 v23, v35, v36 offset0:26 offset1:27
	ds_write2st64_b32 v23, v33, v34 offset0:28 offset1:29
	ds_write2st64_b32 v23, v31, v32 offset0:30 offset1:31
	ds_write2st64_b32 v24, v29, v30 offset0:32 offset1:33
	ds_write2st64_b32 v24, v81, v82 offset0:34 offset1:35
	ds_write2st64_b32 v24, v77, v78 offset0:36 offset1:37
	ds_write2st64_b32 v24, v73, v74 offset0:38 offset1:39
	ds_write2st64_b32 v25, v69, v70 offset0:40 offset1:41
	ds_write2st64_b32 v25, v67, v68 offset0:42 offset1:43
	ds_write2st64_b32 v25, v63, v64 offset0:44 offset1:45
	ds_write2st64_b32 v25, v59, v60 offset0:46 offset1:47
	ds_write2st64_b32 v26, v55, v56 offset0:48 offset1:49
	ds_write2st64_b32 v26, v51, v52 offset0:50 offset1:51
	global_load_dword v159, v[16:17], off nt
	ds_write2st64_b32 v26, v38, v39 offset0:52 offset1:53
	ds_write2st64_b32 v26, v40, v42 offset0:54 offset1:55
	ds_write2st64_b32 v27, v37, v41 offset0:56 offset1:57
	ds_write2st64_b32 v27, v43, v44 offset0:58 offset1:59
	ds_write2st64_b32 v27, v47, v48 offset0:60 offset1:61
	ds_write2st64_b32 v27, v49, v50 offset0:62 offset1:63
	s_waitcnt lgkmcnt(0)
	ds_read2_b32 v[16:17], v1 offset1:32
	v_mov_b32_e32 v30, 0
	ds_read2_b32 v[32:33], v1 offset0:128 offset1:160
	v_mov_b32_e32 v31, 0
	v_add_u32_e32 v145, 0x400, v1
	s_waitcnt lgkmcnt(1)
	v_mul_f32_e32 v4, 0x42800000, v16
	v_mul_f32_e32 v15, 0x42800000, v17
	ds_read2_b32 v[16:17], v1 offset0:64 offset1:96
	v_cvt_pk_fp8_f32 v30, v4, v15
	ds_read2_b32 v[34:35], v145 offset0:128 offset1:160
	v_add_u32_e32 v150, 0x400, v9
	ds_read2_b32 v[38:39], v150 offset0:128 offset1:160
	s_waitcnt lgkmcnt(2)
	v_mul_f32_e32 v4, 0x42800000, v16
	v_mul_f32_e32 v15, 0x42800000, v17
	ds_read2_b32 v[16:17], v1 offset0:192 offset1:224
	v_cvt_pk_fp8_f32 v30, v4, v15 op_sel:[0,0,1]
	v_mul_f32_e32 v4, 0x42800000, v32
	v_mul_f32_e32 v15, 0x42800000, v33
	v_cvt_pk_fp8_f32 v31, v4, v15
	s_waitcnt lgkmcnt(0)
	v_mul_f32_e32 v4, 0x42800000, v16
	v_mul_f32_e32 v15, 0x42800000, v17
	ds_read2_b32 v[16:17], v145 offset0:64 offset1:96
	ds_read2_b32 v[32:33], v145 offset1:32
	v_cvt_pk_fp8_f32 v31, v4, v15 op_sel:[0,0,1]
	v_lshl_add_u64 v[10:11], v[10:11], 0, v[6:7]
	v_add_u32_e32 v156, 0x400, v18
	s_waitcnt lgkmcnt(1)
	v_mul_f32_e32 v29, 0x42800000, v16
	v_mul_f32_e32 v36, 0x42800000, v17
	ds_read2_b32 v[16:17], v145 offset0:192 offset1:224
	s_waitcnt lgkmcnt(1)
	v_mul_f32_e32 v4, 0x42800000, v32
	v_mul_f32_e32 v15, 0x42800000, v33
	v_mov_b32_e32 v32, 0
	v_cvt_pk_fp8_f32 v32, v4, v15
	v_mul_f32_e32 v4, 0x42800000, v34
	v_mul_f32_e32 v15, 0x42800000, v35
	v_mov_b32_e32 v33, 0
	ds_read2_b32 v[34:35], v9 offset1:32
	v_cvt_pk_fp8_f32 v33, v4, v15
	s_waitcnt lgkmcnt(1)
	v_mul_f32_e32 v4, 0x42800000, v16
	v_mul_f32_e32 v15, 0x42800000, v17
	ds_read2_b32 v[16:17], v9 offset0:64 offset1:96
	v_cvt_pk_fp8_f32 v32, v29, v36 op_sel:[0,0,1]
	ds_read2_b32 v[36:37], v9 offset0:128 offset1:160
	v_cvt_pk_fp8_f32 v33, v4, v15 op_sel:[0,0,1]
	s_waitcnt lgkmcnt(2)
	v_mul_f32_e32 v4, 0x42800000, v34
	v_mul_f32_e32 v15, 0x42800000, v35
	v_mov_b32_e32 v34, 0
	v_cvt_pk_fp8_f32 v34, v4, v15
	s_waitcnt lgkmcnt(1)
	v_mul_f32_e32 v4, 0x42800000, v16
	v_mul_f32_e32 v15, 0x42800000, v17
	ds_read2_b32 v[16:17], v9 offset0:192 offset1:224
	s_waitcnt lgkmcnt(1)
	v_mul_f32_e32 v29, 0x42800000, v36
	v_mul_f32_e32 v36, 0x42800000, v37
	v_mov_b32_e32 v35, 0
	v_cvt_pk_fp8_f32 v35, v29, v36
	ds_read2_b32 v[36:37], v150 offset1:32
	v_cvt_pk_fp8_f32 v34, v4, v15 op_sel:[0,0,1]
	s_waitcnt lgkmcnt(1)
	v_mul_f32_e32 v4, 0x42800000, v16
	v_mul_f32_e32 v15, 0x42800000, v17
	ds_read2_b32 v[16:17], v150 offset0:64 offset1:96
	v_cvt_pk_fp8_f32 v35, v4, v15 op_sel:[0,0,1]
	s_waitcnt lgkmcnt(1)
	v_mul_f32_e32 v4, 0x42800000, v36
	v_mul_f32_e32 v15, 0x42800000, v37
	v_mov_b32_e32 v36, 0
	v_cvt_pk_fp8_f32 v36, v4, v15
	s_waitcnt lgkmcnt(0)
	v_mul_f32_e32 v4, 0x42800000, v16
	v_mul_f32_e32 v15, 0x42800000, v17
	ds_read2_b32 v[16:17], v150 offset0:192 offset1:224
	v_cvt_pk_fp8_f32 v36, v4, v15 op_sel:[0,0,1]
	v_mul_f32_e32 v4, 0x42800000, v38
	v_mul_f32_e32 v15, 0x42800000, v39
	v_mov_b32_e32 v37, 0
	v_cvt_pk_fp8_f32 v37, v4, v15
	s_waitcnt lgkmcnt(0)
; __device__ __forceinline__ MoeItem moe_item(const float* wg, const float* wu, const float* wd, const float* win, const float* wout, const float* wpn, const float* wpd, unsigned char* ws, int r, int lane) {
;     if (r >= NMOE_X + NGATE_IT + NWO_IT) { const int q = r - NMOE_X - NGATE_IT - NWO_IT, which = q >> 9, kb = (q >> 6) & 7, nb = q & 63; MoeItem it; it.stride = DM; it.dpitch = 1024;
;         it.src = (which ? wpd : wpn) + (size_t)(kb * 128 + (lane >> 5)) * DM + nb * 32 + (lane & 31);
;         it.dst = ws + (which ? WS_WPDFT : WS_WPNAT) + (size_t)(nb * 32) * 1024 + kb * 128 + (size_t)(lane >> 3) * 1024 + 16 * (lane & 7); return it; }
;     if (r >= NMOE_X + NGATE_IT) { const int q = r - NMOE_X - NGATE_IT, kb = q >> 6, nb = q & 63; MoeItem it; it.stride = DM; it.dpitch = DM;
;         it.src = wout + (size_t)(kb * 128 + (lane >> 5)) * DM + nb * 32 + (lane & 31);
;         it.dst = ws + WS_WO8 + (size_t)(nb * 32) * DM + kb * 128 + (size_t)(lane >> 3) * DM + 16 * (lane & 7); return it; }
;     if (r >= NMOE_X) { const int q = r - NMOE_X, kb = q / 192, nb = q % 192; MoeItem it; it.stride = INC; it.dpitch = DM;
;         const int scol = nb < 128 ? 6144 + nb * 32 : (nb < 160 ? 1024 + (nb - 128) * 32 : 3072 + (nb - 160) * 32);
;         it.src = win + (size_t)(kb * 128 + (lane >> 5)) * INC + scol + (lane & 31);
;         it.dst = ws + WS_WG8 + (size_t)(nb * 32) * DM + kb * 128 + (size_t)(lane >> 3) * DM + 16 * (lane & 7); return it; }
;     const int mat = r / MOE_IE, q = r % MOE_IE, e = mat / 3, which = mat % 3, kb = q / 64, nb = q % 64, n0 = nb * 32;
;     const float* src = (which == 0 ? wg : (which == 1 ? wu : wd)) + (size_t)e * DM * DFF + (size_t)(kb * 128 + (lane >> 5)) * DFF + n0 + (lane & 31);
;     unsigned char* dst;
;     if (which < 2) dst = ws + WS_WGUT + ((size_t)(e * 16 + (n0 >> 7)) * 256 + which * 128 + (n0 & 127)) * DM;
;     else dst = ws + WS_WDT + ((size_t)e * DM + n0) * DFF;
;     MoeItem it; it.stride = DFF; it.dpitch = DM; it.src = src; it.dst = dst + kb * 128 + (size_t)(lane >> 3) * DM + 16 * (lane & 7); return it;
	v_mul_f32_e32 v4, 0x42800000, v16
	v_mul_f32_e32 v15, 0x42800000, v17
	ds_read2_b32 v[16:17], v18 offset1:32
	v_cvt_pk_fp8_f32 v37, v4, v15 op_sel:[0,0,1]
	global_store_dwordx4 v[10:11], v[30:33], off sc0 sc1 nt
	ds_read2_b32 v[32:33], v18 offset0:64 offset1:96
	s_lshl_b64 s[38:39], s[38:39], 3
	s_waitcnt lgkmcnt(1)
	v_mul_f32_e32 v4, 0x42800000, v16
	v_mul_f32_e32 v15, 0x42800000, v17
	ds_read2_b32 v[16:17], v18 offset0:128 offset1:160
	v_mov_b32_e32 v30, 0
	v_cvt_pk_fp8_f32 v30, v4, v15
	s_waitcnt lgkmcnt(1)
	v_mul_f32_e32 v4, 0x42800000, v32
	v_mov_b32_e32 v31, 0
	s_waitcnt lgkmcnt(0)
	v_mul_f32_e32 v29, 0x42800000, v16
	v_mul_f32_e32 v32, 0x42800000, v17
	ds_read2_b32 v[16:17], v18 offset0:192 offset1:224
	v_mul_f32_e32 v15, 0x42800000, v33
	v_cvt_pk_fp8_f32 v31, v29, v32
	ds_read2_b32 v[32:33], v156 offset1:32
	v_cvt_pk_fp8_f32 v30, v4, v15 op_sel:[0,0,1]
	s_waitcnt lgkmcnt(1)
	v_mul_f32_e32 v4, 0x42800000, v16
	v_mul_f32_e32 v15, 0x42800000, v17
	ds_read2_b32 v[16:17], v156 offset0:64 offset1:96
	v_lshl_add_u64 v[10:11], v[10:11], 0, s[38:39]
	global_store_dwordx4 v[10:11], v[34:37], off sc0 sc1 nt
	ds_read2_b32 v[34:35], v156 offset0:128 offset1:160
	v_cvt_pk_fp8_f32 v31, v4, v15 op_sel:[0,0,1]
	s_waitcnt lgkmcnt(2)
	v_mul_f32_e32 v4, 0x42800000, v32
	v_mul_f32_e32 v15, 0x42800000, v33
	v_mov_b32_e32 v32, 0
	v_cvt_pk_fp8_f32 v32, v4, v15
	s_waitcnt lgkmcnt(1)
	v_mul_f32_e32 v4, 0x42800000, v16
	v_mul_f32_e32 v15, 0x42800000, v17
	ds_read2_b32 v[16:17], v156 offset0:192 offset1:224
	s_waitcnt lgkmcnt(1)
	v_mul_f32_e32 v29, 0x42800000, v34
	v_mul_f32_e32 v34, 0x42800000, v35
	v_mov_b32_e32 v33, 0
	v_cvt_pk_fp8_f32 v33, v29, v34
	ds_read2_b32 v[34:35], v19 offset1:32
	v_cvt_pk_fp8_f32 v32, v4, v15 op_sel:[0,0,1]
	s_waitcnt lgkmcnt(1)
	v_mul_f32_e32 v4, 0x42800000, v16
	v_mul_f32_e32 v15, 0x42800000, v17
	ds_read2_b32 v[16:17], v19 offset0:64 offset1:96
	ds_read2_b32 v[36:37], v19 offset0:128 offset1:160
	v_cvt_pk_fp8_f32 v33, v4, v15 op_sel:[0,0,1]
	s_waitcnt lgkmcnt(2)
	v_mul_f32_e32 v4, 0x42800000, v34
	v_mul_f32_e32 v15, 0x42800000, v35
	v_mov_b32_e32 v34, 0
	v_cvt_pk_fp8_f32 v34, v4, v15
	s_waitcnt lgkmcnt(1)
	v_mul_f32_e32 v4, 0x42800000, v16
	v_mul_f32_e32 v15, 0x42800000, v17
	ds_read2_b32 v[16:17], v19 offset0:192 offset1:224
	s_waitcnt lgkmcnt(1)
	v_mul_f32_e32 v29, 0x42800000, v36
	v_mul_f32_e32 v36, 0x42800000, v37
	v_mov_b32_e32 v35, 0
	v_add_u32_e32 v160, 0x400, v19
	v_cvt_pk_fp8_f32 v35, v29, v36
	ds_read2_b32 v[36:37], v160 offset1:32
	v_cvt_pk_fp8_f32 v34, v4, v15 op_sel:[0,0,1]
	s_waitcnt lgkmcnt(1)
	v_mul_f32_e32 v4, 0x42800000, v16
	v_mul_f32_e32 v15, 0x42800000, v17
	ds_read2_b32 v[16:17], v160 offset0:64 offset1:96
	ds_read2_b32 v[38:39], v160 offset0:128 offset1:160
	v_cvt_pk_fp8_f32 v35, v4, v15 op_sel:[0,0,1]
	s_waitcnt lgkmcnt(2)
	v_mul_f32_e32 v4, 0x42800000, v36
	v_mul_f32_e32 v15, 0x42800000, v37
	v_mov_b32_e32 v36, 0
	v_cvt_pk_fp8_f32 v36, v4, v15
	s_waitcnt lgkmcnt(1)
	v_mul_f32_e32 v4, 0x42800000, v16
	v_mul_f32_e32 v15, 0x42800000, v17
	ds_read2_b32 v[16:17], v160 offset0:192 offset1:224
	s_waitcnt lgkmcnt(1)
	v_mul_f32_e32 v29, 0x42800000, v38
	v_mul_f32_e32 v38, 0x42800000, v39
	v_mov_b32_e32 v37, 0
	v_cvt_pk_fp8_f32 v37, v29, v38
	v_cvt_pk_fp8_f32 v36, v4, v15 op_sel:[0,0,1]
	s_waitcnt lgkmcnt(0)
	v_mul_f32_e32 v4, 0x42800000, v16
	v_mul_f32_e32 v15, 0x42800000, v17
	v_cvt_pk_fp8_f32 v37, v4, v15 op_sel:[0,0,1]
	v_lshl_add_u64 v[10:11], v[10:11], 0, s[38:39]
	global_store_dwordx4 v[10:11], v[30:33], off sc0 sc1 nt
	v_lshl_add_u64 v[10:11], v[10:11], 0, s[38:39]
	global_store_dwordx4 v[10:11], v[34:37], off sc0 sc1 nt
	s_waitcnt lgkmcnt(0)
	s_add_i32 s3, s89, s3
	s_min_i32 s43, s3, s7
	s_cmp_lt_i32 s43, 0x19000
	s_mov_b64 s[38:39], -1
	s_cbranch_scc0 .LBB0_126
	s_cmp_lt_i32 s43, 0x18c00
	s_cbranch_scc0 .LBB0_123
	s_cmp_lt_i32 s43, 0x18000
	s_cbranch_scc0 .LBB0_113
	s_ashr_i32 s4, s43, 31
	s_lshr_b32 s4, s4, 22
	s_add_i32 s4, s43, s4
	s_ashr_i32 s39, s4, 10
	s_and_b32 s4, s4, 0xfc00
	s_sub_i32 s46, s43, s4
	s_mul_hi_i32 s4, s43, 0x2aaaaaab
	s_lshr_b32 s38, s4, 31
	s_ashr_i32 s4, s4, 9
	s_add_i32 s38, s4, s38
	s_mul_hi_i32 s4, s39, 0x55555556
	s_lshr_b32 s45, s4, 31
	s_add_i32 s4, s4, s45
	s_mul_i32 s4, s4, 3
	s_sub_i32 s4, s39, s4
	s_sext_i32_i16 s39, s46
	s_bfe_u32 s39, s39, 0x60019
	s_add_i32 s45, s46, s39
	s_and_b32 s39, s45, 0xffc0
	s_sub_i32 s39, s46, s39
	s_sext_i32_i16 s84, s39
	s_lshl_b32 s46, s84, 5
	s_ashr_i32 s39, s38, 31
	s_ashr_i32 s47, s46, 31
	s_cmp_gt_i32 s4, 1
	s_mov_b64 s[70:71], -1
	s_cbranch_scc0 .LBB0_110
	s_lshl_b64 s[68:69], s[38:39], 22
	s_lshl_b64 s[70:71], s[46:47], 11
	s_add_u32 s68, s73, s68
	s_addc_u32 s69, s74, s69
	s_add_u32 s68, s68, s70
	s_addc_u32 s69, s69, s71
	s_mov_b64 s[70:71], 0
